# speedup vs baseline: 1.0015x; 1.0015x over previous
.LBB1_235:
	s_setprio 3
	v_add_u32_e32 v0, s66, v0
	v_subrev_u32_e32 v0, 0x100, v0
	s_movk_i32 s0, 0xf0
	v_cmp_gt_u32_e32 vcc, s0, v0
	s_and_saveexec_b64 s[0:1], vcc
	s_cbranch_execz .Lepi_idle
	s_load_dwordx4 s[68:71], s[14:15], 0x0
	s_load_dwordx2 s[72:73], s[14:15], 0x10
	s_movk_i32 s0, 0x77
	v_mov_b32_e32 v1, 0xffffff88
	v_cmp_lt_u32_e32 vcc, s0, v0
	v_mov_b32_e32 v2, 0x44704000
	s_mov_b32 s0, 0xf800000
	v_cndmask_b32_e32 v1, 0, v1, vcc
	v_add_u32_e32 v0, v1, v0
	v_cvt_f32_u32_e32 v1, v0
	s_mov_b32 s5, 0x17800
	s_mov_b32 s4, 0x3eb17218
	v_fmac_f32_e32 v2, 0xc1000000, v1
	v_sqrt_f32_e32 v1, v2
	s_nop 0
	v_sub_f32_e32 v1, 0x41f80000, v1
	v_mul_f32_e32 v1, 0.5, v1
	v_cvt_i32_f32_e32 v1, v1
	s_and_b64 s[0:1], exec, s[16:17]
	s_cselect_b32 s2, s40, s38
	s_cselect_b32 s3, s39, s33
	v_sub_u32_e32 v2, 31, v1
	v_mul_u32_u24_e32 v2, v2, v1
	v_lshrrev_b32_e32 v2, 1, v2
	v_cmp_gt_i32_e64 s[0:1], v2, v0
	s_nop 1
	v_subbrev_co_u32_e64 v1, s[0:1], 0, v1, s[0:1]
	v_add_u32_e32 v2, 1, v1
	v_sub_u32_e32 v3, 30, v1
	v_mul_u32_u24_e32 v3, v2, v3
	v_lshrrev_b32_e32 v3, 1, v3
	v_cmp_gt_i32_e64 s[0:1], v3, v0
	s_nop 1
	v_cndmask_b32_e64 v12, v2, v1, s[0:1]
	v_sub_u32_e32 v1, 31, v12
	v_mul_u32_u24_e32 v1, v1, v12
	v_lshrrev_b32_e32 v1, 1, v1
	v_sub_u32_e32 v0, v0, v1
	v_cndmask_b32_e64 v1, 0, 16, vcc
	v_lshl_or_b32 v1, s2, 5, v1
	v_add_u32_e32 v1, v1, v12
	v_sub_u32_e32 v2, 0xff, v1
	v_mul_u32_u24_e32 v1, v2, v1
	v_lshrrev_b32_e32 v1, 1, v1
	v_add3_u32 v13, v12, v0, 1
	v_add_u32_e32 v0, v1, v0
	s_mul_i32 s3, s3, 0x1fc0
	v_add_u32_e32 v0, s3, v0
	v_mul_u32_u24_e32 v4, 24, v0
	v_mov_b32_e32 v0, 0x17800
	v_lshl_add_u32 v14, v12, 2, v0
	v_mov_b32_e32 v0, 0x60
	v_cndmask_b32_e32 v15, 0, v0, vcc
	v_lshlrev_b32_e32 v16, 2, v13
	v_add_lshl_u32 v0, v15, v12, 6
	v_add3_u32 v16, v0, v16, s5
	v_add_u32_e32 v1, v15, v13
	v_lshl_add_u32 v17, v1, 6, v14
	ds_read_b32 v0, v16
	ds_read_b32 v2, v17
	ds_read_b32 v1, v16 offset:1024
	ds_read_b32 v3, v17 offset:1024
	ds_read_b32 v6, v16 offset:2048
	ds_read_b32 v8, v17 offset:2048
	ds_read_b32 v7, v16 offset:3072
	ds_read_b32 v9, v17 offset:3072
	ds_read_b32 v12, v16 offset:4096
	ds_read_b32 v14, v17 offset:4096
	ds_read_b32 v13, v16 offset:5120
	ds_read_b32 v15, v17 offset:5120
	s_waitcnt lgkmcnt(0)
	v_pk_add_f32 v[0:1], v[0:1], v[2:3]
	v_mov_b32_e32 v2, s70
	v_mov_b32_e32 v3, s71
	v_mov_b64_e32 v[10:11], s[68:69]
	v_pk_add_f32 v[6:7], v[6:7], v[8:9]
	v_pk_fma_f32 v[0:1], v[0:1], s[4:5], v[10:11] op_sel_hi:[1,0,1]
	v_pk_fma_f32 v[2:3], v[6:7], s[4:5], v[2:3] op_sel_hi:[1,0,1]
	global_store_dwordx4 v4, v[0:3], s[10:11]
	s_nop 1
	v_pk_add_f32 v[0:1], v[12:13], v[14:15]
	v_mov_b64_e32 v[2:3], s[72:73]
	v_pk_fma_f32 v[0:1], v[0:1], s[4:5], v[2:3] op_sel_hi:[1,0,1]
	global_store_dwordx2 v4, v[0:1], s[10:11] offset:16
	s_endpgm
